# speedup vs baseline: 1.5356x; 1.0086x over previous
_Z6scan_kPKDF16_S0_S0_S0_PKfPf:
	s_load_dwordx8 s[4:11], s[0:1], 0x0
	s_load_dwordx4 s[12:15], s[0:1], 0x20
	v_and_b32_e32 v1, 63, v0
	v_lshrrev_b32_e32 v2, 6, v0
	s_nop 1
	v_readfirstlane_b32 s16, v2
	s_lshr_b32 s17, s2, 7
	s_and_b32 s18, s2, 127
	s_lshl_b32 s18, s18, 2
	s_add_u32 s18, s18, s16
	s_lshl_b32 s19, s17, 9
	s_add_u32 s19, s19, s18
	s_mul_i32 s28, s16, 4608
	s_add_u32 s28, s28, 67584
	s_lshl_b32 s32, s16, 10
	s_add_u32 s33, s32, 0x1000
	s_add_u32 s34, s32, 0x2000
	s_add_u32 s35, s32, 0x3000
	s_mov_b32 s46, 0x200
	s_mov_b32 s47, 0
	s_mov_b32 s40, 0
	v_lshlrev_b32_e32 v2, 4, v1
	v_add_u32_e32 v3, 0x1000, v2
	v_add_u32_e32 v4, 0x2000, v2
	v_add_u32_e32 v5, 0x3000, v2
	v_lshlrev_b32_e32 v6, 2, v1
	v_lshlrev_b32_e32 v7, 1, v1
	v_and_b32_e32 v20, 7, v1
	v_lshlrev_b32_e32 v20, 1, v20
	v_add_u32_e32 v8, v2, v20
	v_add_u32_e32 v8, s28, v8
	v_and_b32_e32 v20, 3, v1
	v_bfe_u32 v21, v1, 3, 2
	v_lshl_add_u32 v20, v21, 2, v20
	v_lshrrev_b32_e32 v21, 5, v1
	v_bfe_u32 v22, v1, 2, 1
	v_bfe_u32 v23, v1, 4, 1
	v_cmp_eq_u32_e64 s[48:49], v21, v22
	v_cmp_eq_u32_e64 s[50:51], 0, v23
	s_nop 1
	s_and_b64 s[52:53], s[48:49], s[50:51]
	s_andn2_b64 s[54:55], s[48:49], s[50:51]
	v_mov_b32_e32 v24, 65536
	v_lshlrev_b32_e32 v25, 1, v20
	v_add_u32_e32 v25, s28, v25
	v_add_u32_e32 v26, 0x100, v25
	s_nop 1
	v_cndmask_b32_e64 v9, v24, v25, s[48:49]
	v_cndmask_b32_e64 v10, v24, v26, s[48:49]
	v_lshlrev_b32_e32 v25, 4, v20
	v_add_u32_e32 v25, s28, v25
	v_add_u32_e32 v25, 0x200, v25
	v_add_u32_e32 v26, 0x800, v25
	v_cndmask_b32_e64 v11, v24, v25, s[48:49]
	v_cndmask_b32_e64 v13, v24, v26, s[48:49]
	v_mov_b32_e32 v15, 1.0
	v_and_b32_e32 v89, 15, v1
	s_mov_b32 s42, 0xffff
	s_mov_b32 s43, 0
	v_xor_b32_e32 v86, 16, v1
	v_lshlrev_b32_e32 v86, 2, v86
	v_xor_b32_e32 v87, 32, v1
	v_lshlrev_b32_e32 v87, 2, v87
	s_waitcnt lgkmcnt(0)
	s_lshl_b32 s30, s19, 13
	s_add_u32 s24, s4, s30
	s_addc_u32 s25, s5, 0
	s_add_u32 s26, s6, s30
	s_addc_u32 s27, s7, 0
	s_lshl_b32 s30, s17, 19
	s_add_u32 s30, s30, s32
	s_add_u32 s20, s8, s30
	s_addc_u32 s21, s9, 0
	s_add_u32 s22, s10, s30
	s_addc_u32 s23, s11, 0
	s_lshl_b32 s30, s18, 8
	s_add_u32 s12, s12, s30
	s_addc_u32 s13, s13, 0
	global_load_dword v90, v6, s[12:13]
	global_load_ushort v18, v7, s[26:27]
	global_load_ushort v19, v7, s[26:27] offset:128
	s_lshl_b32 s30, s19, 14
	s_add_u32 s14, s14, s30
	s_addc_u32 s15, s15, 0
	v_and_b32_e32 v30, 15, v1
	v_lshlrev_b32_e32 v30, 2, v30
	v_mov_b32_e32 v31, 0
	v_lshl_add_u64 v[16:17], s[14:15], 0, v[30:31]
	v_mov_b32_e32 v36, 0
	v_mov_b32_e32 v37, 0
	v_mov_b32_e32 v38, 0
	v_mov_b32_e32 v39, 0
	v_add_u32_e32 v29, 65536, v2
	ds_write_b128 v29, v[36:39]
	ds_write_b128 v29, v[36:39] offset:1024
	v_add_u32_e32 v29, s28, v2
	ds_write_b128 v29, v[36:39] offset:512
	ds_write_b128 v29, v[36:39] offset:1536
	ds_write_b128 v29, v[36:39] offset:2560
	ds_write_b128 v29, v[36:39] offset:3584
	s_mov_b32 m0, s32
	s_nop 0
	global_load_lds_dwordx4 v2, s[20:21]
	s_add_i32 m0, s32, 32768
	s_nop 0
	global_load_lds_dwordx4 v2, s[22:23]
	s_mov_b32 m0, s33
	s_nop 0
	global_load_lds_dwordx4 v3, s[20:21]
	s_add_i32 m0, s33, 32768
	s_nop 0
	global_load_lds_dwordx4 v3, s[22:23]
	s_mov_b32 m0, s34
	s_nop 0
	global_load_lds_dwordx4 v4, s[20:21]
	s_add_i32 m0, s34, 32768
	s_nop 0
	global_load_lds_dwordx4 v4, s[22:23]
	s_mov_b32 m0, s35
	s_nop 0
	global_load_lds_dwordx4 v5, s[20:21]
	s_add_i32 m0, s35, 32768
	s_nop 0
	global_load_lds_dwordx4 v5, s[22:23]
	s_mov_b32 m0, s28
	s_nop 0
	global_load_lds_dword v6, s[24:25]
	s_add_u32 s20, s20, 0x4000
	s_addc_u32 s21, s21, 0
	s_add_u32 s22, s22, 0x4000
	s_addc_u32 s23, s23, 0
	s_add_u32 s24, s24, 0x100
	s_addc_u32 s25, s25, 0
	s_add_i32 m0, s32, 16384
	s_nop 0
	global_load_lds_dwordx4 v2, s[20:21]
	s_add_i32 m0, s32, 49152
	s_nop 0
	global_load_lds_dwordx4 v2, s[22:23]
	s_add_i32 m0, s33, 16384
	s_nop 0
	global_load_lds_dwordx4 v3, s[20:21]
	s_add_i32 m0, s33, 49152
	s_nop 0
	global_load_lds_dwordx4 v3, s[22:23]
	s_add_i32 m0, s34, 16384
	s_nop 0
	global_load_lds_dwordx4 v4, s[20:21]
	s_add_i32 m0, s34, 49152
	s_nop 0
	global_load_lds_dwordx4 v4, s[22:23]
	s_add_i32 m0, s35, 16384
	s_nop 0
	global_load_lds_dwordx4 v5, s[20:21]
	s_add_i32 m0, s35, 49152
	s_nop 0
	global_load_lds_dwordx4 v5, s[22:23]
	s_add_i32 m0, s28, 0x100
	s_nop 0
	global_load_lds_dword v6, s[24:25]
	s_add_u32 s20, s20, 0x4000
	s_addc_u32 s21, s21, 0
	s_add_u32 s22, s22, 0x4000
	s_addc_u32 s23, s23, 0
	s_add_u32 s24, s24, 0x100
	s_addc_u32 s25, s25, 0
	s_mov_b32 s3, 0x3fb8aa3b
	s_waitcnt vmcnt(20)
	v_mul_f32_e32 v91, 0x3fb8aa3b, v90
	v_fma_f32 v92, v90, s3, -v91
	v_rndne_f32_e32 v93, v91
	v_fmamk_f32 v92, v90, 0x32a5705f, v92
	v_sub_f32_e32 v91, v91, v93
	v_add_f32_e32 v91, v91, v92
	v_exp_f32_e32 v91, v91
	v_cvt_i32_f32_e32 v92, v93
	s_mov_b32 s3, 0xc2ce8ed0
	v_cmp_ngt_f32_e32 vcc, s3, v90
	s_mov_b32 s3, 0x42b17218
	v_ldexp_f32 v91, v91, v92
	v_cndmask_b32_e32 v91, 0, v91, vcc
	v_mov_b32_e32 v92, 0x7f800000
	v_cmp_nlt_f32_e32 vcc, s3, v90
	s_mov_b32 s3, 0xbfb8aa3b
	s_nop 1
	v_cndmask_b32_e32 v90, v92, v91, vcc
	v_mov_b32_e32 v93, 0
	s_nop 0
	v_fma_mixlo_f16 v93, v90, s3, 0
	v_and_b32_e32 v28, 0xffff, v93
	v_mov_b32_e32 v29, 0
	v_mov_b32_e32 v30, 0
	v_mov_b32_e32 v31, 0
	v_mov_b32_e32 v32, 0
	v_mov_b32_e32 v33, 0
	v_mov_b32_e32 v34, 0
	v_mov_b32_e32 v35, 0
	v_mov_b32_e32 v96, 0x1c00
	v_mov_b32_e32 v97, 0x1c000000
	v_cmp_eq_u32_e32 vcc, 0, v89
	s_nop 1
	v_cndmask_b32_e32 v20, 0, v96, vcc
	v_cmp_eq_u32_e32 vcc, 1, v89
	s_nop 1
	v_cndmask_b32_e32 v20, v20, v97, vcc
	v_cmp_eq_u32_e32 vcc, 2, v89
	s_nop 1
	v_cndmask_b32_e32 v21, 0, v96, vcc
	v_cmp_eq_u32_e32 vcc, 3, v89
	s_nop 1
	v_cndmask_b32_e32 v21, v21, v97, vcc
	v_cmp_eq_u32_e32 vcc, 4, v89
	s_nop 1
	v_cndmask_b32_e32 v22, 0, v96, vcc
	v_cmp_eq_u32_e32 vcc, 5, v89
	s_nop 1
	v_cndmask_b32_e32 v22, v22, v97, vcc
	v_cmp_eq_u32_e32 vcc, 6, v89
	s_nop 1
	v_cndmask_b32_e32 v23, 0, v96, vcc
	v_cmp_eq_u32_e32 vcc, 7, v89
	s_nop 1
	v_cndmask_b32_e32 v23, v23, v97, vcc
	v_cmp_eq_u32_e32 vcc, 8, v89
	s_nop 1
	v_cndmask_b32_e32 v24, 0, v96, vcc
	v_cmp_eq_u32_e32 vcc, 9, v89
	s_nop 1
	v_cndmask_b32_e32 v24, v24, v97, vcc
	v_cmp_eq_u32_e32 vcc, 10, v89
	s_nop 1
	v_cndmask_b32_e32 v25, 0, v96, vcc
	v_cmp_eq_u32_e32 vcc, 11, v89
	s_nop 1
	v_cndmask_b32_e32 v25, v25, v97, vcc
	v_cmp_eq_u32_e32 vcc, 12, v89
	s_nop 1
	v_cndmask_b32_e32 v26, 0, v96, vcc
	v_cmp_eq_u32_e32 vcc, 13, v89
	s_nop 1
	v_cndmask_b32_e32 v26, v26, v97, vcc
	v_cmp_eq_u32_e32 vcc, 14, v89
	s_nop 1
	v_cndmask_b32_e32 v27, 0, v96, vcc
	v_cmp_eq_u32_e32 vcc, 15, v89
	s_nop 1
	v_cndmask_b32_e32 v27, v27, v97, vcc
	v_mov_b32_e32 v191, 0
	v_mov_b32_e32 v85, 0
	v_mov_b32_e32 v88, 0
	v_mov_b32_e32 v84, 0
	v_mov_b32_e32 v68, 0
	v_mov_b32_e32 v69, 0
	v_mov_b32_e32 v70, 0
	v_mov_b32_e32 v71, 0
	v_mov_b32_e32 v72, 0
	v_mov_b32_e32 v73, 0
	v_mov_b32_e32 v74, 0
	v_mov_b32_e32 v75, 0
	v_mov_b32_e32 v76, 0
	v_mov_b32_e32 v77, 0
	v_mov_b32_e32 v78, 0
	v_mov_b32_e32 v79, 0
	v_mov_b32_e32 v80, 0
	v_mov_b32_e32 v81, 0
	v_mov_b32_e32 v82, 0
	v_mov_b32_e32 v83, 0
	s_waitcnt vmcnt(18)
	v_add_u32_e32 v8, 0x200, v8
	v_add_u32_e32 v94, 0x800, v8
	v_mov_b32_e32 v92, v2
	v_add_u32_e32 v93, 0x4000, v2
	s_mov_b32 s29, s28
	ds_write_b16 v8, v18
	ds_write_b16 v8, v19 offset:1024
	s_add_u32 s26, s26, 0x100
	s_addc_u32 s27, s27, 0
	global_load_ushort v18, v7, s[26:27]
	global_load_ushort v19, v7, s[26:27] offset:128
	s_add_u32 s26, s26, 0x100
	s_addc_u32 s27, s27, 0
	s_waitcnt vmcnt(0)
	s_waitcnt lgkmcnt(0)
	s_barrier
	ds_read_b128 v[52:55], v92 offset:32768
	ds_read_b128 v[56:59], v92 offset:33792
	ds_read_u16 v32, v9 offset:0
	ds_read_b128 v[36:39], v11 offset:0
	ds_read_b128 v[44:47], v92 offset:0
	ds_read_b128 v[48:51], v92 offset:1024
	s_waitcnt lgkmcnt(0)
	v_mfma_f32_32x32x8_f16 v[96:111], v[32:33], v[28:29], 0
	v_mfma_f32_32x32x16_f16 v[128:143], v[36:39], v[44:47], 0
	v_mfma_f32_32x32x16_f16 v[160:175], v[36:39], v[48:51], 0
	ds_read_u16 v32, v9 offset:32
	ds_read_b128 v[36:39], v11 offset:256
	ds_read_b128 v[44:47], v92 offset:2048
	ds_read_b128 v[48:51], v92 offset:3072
	s_nop 15
	s_nop 15
.Lscan_loop:
	v_exp_f32_e32 v96, v96
	v_exp_f32_e32 v97, v97
	v_mfma_f32_16x16x32_f16 v[80:83], v[72:75], v[24:27], v[80:83]
	ds_read_b128 v[60:63], v92 offset:34816
	ds_bpermute_b32 v90, v87, v85
	s_waitcnt lgkmcnt(2)
	v_exp_f32_e32 v98, v98
	v_exp_f32_e32 v99, v99
	v_mfma_f32_32x32x8_f16 v[112:127], v[32:33], v[28:29], 0
	ds_read_u16 v32, v9 offset:64
	ds_read_b128 v[64:67], v92 offset:35840
	v_fmac_f32_e32 v128, v96, v191
	v_exp_f32_e32 v100, v100
	v_fmac_f32_e32 v129, v97, v128
	v_exp_f32_e32 v101, v101
	v_fmac_f32_e32 v130, v98, v129
	v_cvt_pkrtz_f16_f32 v68, v128, v129
	v_exp_f32_e32 v102, v102
	v_fmac_f32_e32 v131, v99, v130
	v_pk_mul_f16 v68, v52, v68
	v_exp_f32_e32 v103, v103
	v_add_f32_e32 v84, v80, v81
	v_add_f32_e32 v91, v82, v83
	v_fmac_f32_e32 v132, v100, v131
	v_add_f32_e32 v84, v84, v91
	v_cvt_pkrtz_f16_f32 v69, v130, v131
	v_mfma_f32_32x32x16_f16 v[144:159], v[36:39], v[44:47], 0
	ds_read_b128 v[44:47], v92 offset:4096
	ds_bpermute_b32 v89, v86, v84
	v_exp_f32_e32 v104, v104
	v_fmac_f32_e32 v133, v101, v132
	v_pk_mul_f16 v69, v53, v69
	v_exp_f32_e32 v105, v105
	v_fmac_f32_e32 v134, v102, v133
	v_cvt_pkrtz_f16_f32 v70, v132, v133
	v_exp_f32_e32 v106, v106
	v_fmac_f32_e32 v135, v103, v134
	v_pk_mul_f16 v70, v54, v70
	v_exp_f32_e32 v107, v107
	v_mfma_f32_32x32x16_f16 v[176:191], v[36:39], v[48:51], 0
	ds_read_b128 v[36:39], v11 offset:512
	ds_read_b128 v[48:51], v92 offset:5120
	v_cvt_pkrtz_f16_f32 v71, v134, v135
	v_fmac_f32_e32 v168, v104, v135
	v_pk_mul_f16 v71, v55, v71
	v_exp_f32_e32 v108, v108
	v_fmac_f32_e32 v169, v105, v168
	v_mfma_f32_16x16x32_f16 v[76:79], v[68:71], v[20:23], 0
	v_cvt_pkrtz_f16_f32 v72, v168, v169
	v_exp_f32_e32 v109, v109
	v_fmac_f32_e32 v170, v106, v169
	v_pk_mul_f16 v72, v56, v72
	v_fmac_f32_e32 v171, v107, v170
	v_exp_f32_e32 v110, v110
	v_cvt_pkrtz_f16_f32 v73, v170, v171
	v_fmac_f32_e32 v172, v108, v171
	v_pk_mul_f16 v73, v57, v73
	v_fmac_f32_e32 v173, v109, v172
	v_exp_f32_e32 v111, v111
	v_cvt_pkrtz_f16_f32 v74, v172, v173
	v_fmac_f32_e32 v174, v110, v173
	v_pk_mul_f16 v74, v58, v74
	s_waitcnt lgkmcnt(2)
	v_add_f32_e32 v198, v85, v90
	v_fmac_f32_e32 v175, v111, v174
	v_add_f32_e32 v88, v84, v89
	v_cvt_pkrtz_f16_f32 v75, v174, v175
	v_pk_mul_f16 v75, v59, v75
	v_exp_f32_e32 v112, v112
	v_exp_f32_e32 v113, v113
	v_mfma_f32_16x16x32_f16 v[76:79], v[72:75], v[24:27], v[76:79]
	ds_read_b128 v[52:55], v92 offset:36864
	ds_bpermute_b32 v90, v87, v88
	s_waitcnt lgkmcnt(2)
	v_exp_f32_e32 v114, v114
	v_exp_f32_e32 v115, v115
	v_mfma_f32_32x32x8_f16 v[96:111], v[32:33], v[28:29], 0
	ds_read_u16 v32, v9 offset:96
	ds_read_b128 v[56:59], v92 offset:37888
	v_fmac_f32_e32 v144, v112, v175
	v_exp_f32_e32 v116, v116
	v_fmac_f32_e32 v145, v113, v144
	v_exp_f32_e32 v117, v117
	v_fmac_f32_e32 v146, v114, v145
	v_cvt_pkrtz_f16_f32 v68, v144, v145
	v_exp_f32_e32 v118, v118
	v_fmac_f32_e32 v147, v115, v146
	v_pk_mul_f16 v68, v60, v68
	v_exp_f32_e32 v119, v119
	v_add_f32_e32 v84, v76, v77
	v_add_f32_e32 v91, v78, v79
	v_fmac_f32_e32 v148, v116, v147
	v_add_f32_e32 v84, v84, v91
	v_cvt_pkrtz_f16_f32 v69, v146, v147
	v_mfma_f32_32x32x16_f16 v[128:143], v[36:39], v[44:47], 0
	ds_read_b128 v[44:47], v92 offset:6144
	ds_bpermute_b32 v89, v86, v84
	v_exp_f32_e32 v120, v120
	v_fmac_f32_e32 v149, v117, v148
	v_pk_mul_f16 v69, v61, v69
	v_exp_f32_e32 v121, v121
	v_fmac_f32_e32 v150, v118, v149
	v_cvt_pkrtz_f16_f32 v70, v148, v149
	v_exp_f32_e32 v122, v122
	v_fmac_f32_e32 v151, v119, v150
	v_pk_mul_f16 v70, v62, v70
	v_exp_f32_e32 v123, v123
	v_mfma_f32_32x32x16_f16 v[160:175], v[36:39], v[48:51], 0
	ds_read_b128 v[36:39], v11 offset:768
	ds_read_b128 v[48:51], v92 offset:7168
	v_cvt_pkrtz_f16_f32 v71, v150, v151
	v_fmac_f32_e32 v184, v120, v151
	v_pk_mul_f16 v71, v63, v71
	v_exp_f32_e32 v124, v124
	v_fmac_f32_e32 v185, v121, v184
	v_mfma_f32_16x16x32_f16 v[80:83], v[68:71], v[20:23], 0
	v_cvt_pkrtz_f16_f32 v72, v184, v185
	v_exp_f32_e32 v125, v125
	v_fmac_f32_e32 v186, v122, v185
	v_pk_mul_f16 v72, v64, v72
	v_fmac_f32_e32 v187, v123, v186
	v_exp_f32_e32 v126, v126
	v_cvt_pkrtz_f16_f32 v73, v186, v187
	v_fmac_f32_e32 v188, v124, v187
	v_pk_mul_f16 v73, v65, v73
	v_fmac_f32_e32 v189, v125, v188
	v_exp_f32_e32 v127, v127
	v_cvt_pkrtz_f16_f32 v74, v188, v189
	v_fmac_f32_e32 v190, v126, v189
	v_pk_mul_f16 v74, v66, v74
	s_waitcnt lgkmcnt(2)
	v_add_f32_e32 v199, v88, v90
	v_fmac_f32_e32 v191, v127, v190
	v_add_f32_e32 v85, v84, v89
	v_cvt_pkrtz_f16_f32 v75, v190, v191
	v_pk_mul_f16 v75, v67, v75
	v_exp_f32_e32 v96, v96
	v_exp_f32_e32 v97, v97
	v_mfma_f32_16x16x32_f16 v[80:83], v[72:75], v[24:27], v[80:83]
	ds_read_b128 v[60:63], v92 offset:38912
	ds_bpermute_b32 v90, v87, v85
	s_waitcnt lgkmcnt(2)
	v_exp_f32_e32 v98, v98
	v_exp_f32_e32 v99, v99
	v_mfma_f32_32x32x8_f16 v[112:127], v[32:33], v[28:29], 0
	ds_read_u16 v32, v9 offset:128
	ds_read_b128 v[64:67], v92 offset:39936
	v_fmac_f32_e32 v128, v96, v191
	v_exp_f32_e32 v100, v100
	v_fmac_f32_e32 v129, v97, v128
	v_exp_f32_e32 v101, v101
	v_fmac_f32_e32 v130, v98, v129
	v_cvt_pkrtz_f16_f32 v68, v128, v129
	v_exp_f32_e32 v102, v102
	v_fmac_f32_e32 v131, v99, v130
	v_pk_mul_f16 v68, v52, v68
	v_exp_f32_e32 v103, v103
	v_add_f32_e32 v84, v80, v81
	v_add_f32_e32 v91, v82, v83
	v_fmac_f32_e32 v132, v100, v131
	v_add_f32_e32 v84, v84, v91
	v_cvt_pkrtz_f16_f32 v69, v130, v131
	v_mfma_f32_32x32x16_f16 v[144:159], v[36:39], v[44:47], 0
	ds_read_b128 v[44:47], v92 offset:8192
	ds_bpermute_b32 v89, v86, v84
	v_exp_f32_e32 v104, v104
	v_fmac_f32_e32 v133, v101, v132
	v_pk_mul_f16 v69, v53, v69
	v_exp_f32_e32 v105, v105
	v_fmac_f32_e32 v134, v102, v133
	v_cvt_pkrtz_f16_f32 v70, v132, v133
	v_exp_f32_e32 v106, v106
	v_fmac_f32_e32 v135, v103, v134
	v_pk_mul_f16 v70, v54, v70
	v_exp_f32_e32 v107, v107
	v_mfma_f32_32x32x16_f16 v[176:191], v[36:39], v[48:51], 0
	ds_read_b128 v[36:39], v11 offset:1024
	ds_read_b128 v[48:51], v92 offset:9216
	v_cvt_pkrtz_f16_f32 v71, v134, v135
	v_fmac_f32_e32 v168, v104, v135
	v_pk_mul_f16 v71, v55, v71
	v_exp_f32_e32 v108, v108
	v_fmac_f32_e32 v169, v105, v168
	v_mfma_f32_16x16x32_f16 v[76:79], v[68:71], v[20:23], 0
	v_cvt_pkrtz_f16_f32 v72, v168, v169
	v_exp_f32_e32 v109, v109
	v_fmac_f32_e32 v170, v106, v169
	v_pk_mul_f16 v72, v56, v72
	v_fmac_f32_e32 v171, v107, v170
	v_exp_f32_e32 v110, v110
	v_cvt_pkrtz_f16_f32 v73, v170, v171
	v_fmac_f32_e32 v172, v108, v171
	v_pk_mul_f16 v73, v57, v73
	v_fmac_f32_e32 v173, v109, v172
	v_exp_f32_e32 v111, v111
	v_cvt_pkrtz_f16_f32 v74, v172, v173
	v_fmac_f32_e32 v174, v110, v173
	v_pk_mul_f16 v74, v58, v74
	s_waitcnt lgkmcnt(2)
	v_add_f32_e32 v192, v85, v90
	v_fmac_f32_e32 v175, v111, v174
	v_add_f32_e32 v88, v84, v89
	v_cvt_pkrtz_f16_f32 v75, v174, v175
	v_pk_mul_f16 v75, v59, v75
	v_exp_f32_e32 v112, v112
	v_exp_f32_e32 v113, v113
	v_mfma_f32_16x16x32_f16 v[76:79], v[72:75], v[24:27], v[76:79]
	ds_read_b128 v[52:55], v92 offset:40960
	ds_bpermute_b32 v90, v87, v88
	s_waitcnt lgkmcnt(2)
	v_exp_f32_e32 v114, v114
	v_exp_f32_e32 v115, v115
	v_mfma_f32_32x32x8_f16 v[96:111], v[32:33], v[28:29], 0
	ds_read_u16 v32, v9 offset:160
	ds_read_b128 v[56:59], v92 offset:41984
	v_fmac_f32_e32 v144, v112, v175
	v_exp_f32_e32 v116, v116
	v_fmac_f32_e32 v145, v113, v144
	v_exp_f32_e32 v117, v117
	v_fmac_f32_e32 v146, v114, v145
	v_cvt_pkrtz_f16_f32 v68, v144, v145
	v_exp_f32_e32 v118, v118
	v_fmac_f32_e32 v147, v115, v146
	v_pk_mul_f16 v68, v60, v68
	v_exp_f32_e32 v119, v119
	v_add_f32_e32 v84, v76, v77
	v_add_f32_e32 v91, v78, v79
	v_fmac_f32_e32 v148, v116, v147
	v_add_f32_e32 v84, v84, v91
	v_cvt_pkrtz_f16_f32 v69, v146, v147
	v_mfma_f32_32x32x16_f16 v[128:143], v[36:39], v[44:47], 0
	ds_read_b128 v[44:47], v92 offset:10240
	ds_bpermute_b32 v89, v86, v84
	v_exp_f32_e32 v120, v120
	v_fmac_f32_e32 v149, v117, v148
	v_pk_mul_f16 v69, v61, v69
	v_exp_f32_e32 v121, v121
	v_fmac_f32_e32 v150, v118, v149
	v_cvt_pkrtz_f16_f32 v70, v148, v149
	v_exp_f32_e32 v122, v122
	v_fmac_f32_e32 v151, v119, v150
	v_pk_mul_f16 v70, v62, v70
	v_exp_f32_e32 v123, v123
	v_mfma_f32_32x32x16_f16 v[160:175], v[36:39], v[48:51], 0
	ds_read_b128 v[36:39], v11 offset:1280
	ds_read_b128 v[48:51], v92 offset:11264
	v_cvt_pkrtz_f16_f32 v71, v150, v151
	v_fmac_f32_e32 v184, v120, v151
	v_pk_mul_f16 v71, v63, v71
	v_exp_f32_e32 v124, v124
	v_fmac_f32_e32 v185, v121, v184
	v_mfma_f32_16x16x32_f16 v[80:83], v[68:71], v[20:23], 0
	v_cvt_pkrtz_f16_f32 v72, v184, v185
	v_exp_f32_e32 v125, v125
	v_fmac_f32_e32 v186, v122, v185
	v_pk_mul_f16 v72, v64, v72
	v_fmac_f32_e32 v187, v123, v186
	v_exp_f32_e32 v126, v126
	v_cvt_pkrtz_f16_f32 v73, v186, v187
	v_fmac_f32_e32 v188, v124, v187
	v_pk_mul_f16 v73, v65, v73
	v_fmac_f32_e32 v189, v125, v188
	v_exp_f32_e32 v127, v127
	v_cvt_pkrtz_f16_f32 v74, v188, v189
	v_fmac_f32_e32 v190, v126, v189
	v_pk_mul_f16 v74, v66, v74
	s_waitcnt lgkmcnt(2)
	v_add_f32_e32 v193, v88, v90
	v_fmac_f32_e32 v191, v127, v190
	v_add_f32_e32 v85, v84, v89
	v_cvt_pkrtz_f16_f32 v75, v190, v191
	v_pk_mul_f16 v75, v67, v75
	v_exp_f32_e32 v96, v96
	v_exp_f32_e32 v97, v97
	v_mfma_f32_16x16x32_f16 v[80:83], v[72:75], v[24:27], v[80:83]
	ds_read_b128 v[60:63], v92 offset:43008
	ds_bpermute_b32 v90, v87, v85
	s_waitcnt lgkmcnt(2)
	v_exp_f32_e32 v98, v98
	v_exp_f32_e32 v99, v99
	v_mfma_f32_32x32x8_f16 v[112:127], v[32:33], v[28:29], 0
	ds_read_u16 v32, v9 offset:192
	ds_read_b128 v[64:67], v92 offset:44032
	v_fmac_f32_e32 v128, v96, v191
	v_exp_f32_e32 v100, v100
	v_fmac_f32_e32 v129, v97, v128
	v_exp_f32_e32 v101, v101
	v_fmac_f32_e32 v130, v98, v129
	v_cvt_pkrtz_f16_f32 v68, v128, v129
	v_exp_f32_e32 v102, v102
	v_fmac_f32_e32 v131, v99, v130
	v_pk_mul_f16 v68, v52, v68
	v_exp_f32_e32 v103, v103
	v_add_f32_e32 v84, v80, v81
	v_add_f32_e32 v91, v82, v83
	v_fmac_f32_e32 v132, v100, v131
	v_add_f32_e32 v84, v84, v91
	v_cvt_pkrtz_f16_f32 v69, v130, v131
	v_mfma_f32_32x32x16_f16 v[144:159], v[36:39], v[44:47], 0
	ds_read_b128 v[44:47], v92 offset:12288
	ds_bpermute_b32 v89, v86, v84
	v_exp_f32_e32 v104, v104
	v_fmac_f32_e32 v133, v101, v132
	v_pk_mul_f16 v69, v53, v69
	v_exp_f32_e32 v105, v105
	v_fmac_f32_e32 v134, v102, v133
	v_cvt_pkrtz_f16_f32 v70, v132, v133
	v_exp_f32_e32 v106, v106
	v_fmac_f32_e32 v135, v103, v134
	v_pk_mul_f16 v70, v54, v70
	v_exp_f32_e32 v107, v107
	v_mfma_f32_32x32x16_f16 v[176:191], v[36:39], v[48:51], 0
	ds_read_b128 v[36:39], v11 offset:1536
	ds_read_b128 v[48:51], v92 offset:13312
	v_cvt_pkrtz_f16_f32 v71, v134, v135
	v_fmac_f32_e32 v168, v104, v135
	v_pk_mul_f16 v71, v55, v71
	v_exp_f32_e32 v108, v108
	v_fmac_f32_e32 v169, v105, v168
	v_mfma_f32_16x16x32_f16 v[76:79], v[68:71], v[20:23], 0
	v_cvt_pkrtz_f16_f32 v72, v168, v169
	v_exp_f32_e32 v109, v109
	v_fmac_f32_e32 v170, v106, v169
	v_pk_mul_f16 v72, v56, v72
	v_fmac_f32_e32 v171, v107, v170
	v_exp_f32_e32 v110, v110
	v_cvt_pkrtz_f16_f32 v73, v170, v171
	v_fmac_f32_e32 v172, v108, v171
	v_pk_mul_f16 v73, v57, v73
	v_fmac_f32_e32 v173, v109, v172
	v_exp_f32_e32 v111, v111
	v_cvt_pkrtz_f16_f32 v74, v172, v173
	v_fmac_f32_e32 v174, v110, v173
	v_pk_mul_f16 v74, v58, v74
	s_waitcnt lgkmcnt(2)
	v_add_f32_e32 v194, v85, v90
	v_fmac_f32_e32 v175, v111, v174
	v_add_f32_e32 v88, v84, v89
	v_cvt_pkrtz_f16_f32 v75, v174, v175
	v_pk_mul_f16 v75, v59, v75
	v_exp_f32_e32 v112, v112
	v_exp_f32_e32 v113, v113
	v_mfma_f32_16x16x32_f16 v[76:79], v[72:75], v[24:27], v[76:79]
	ds_read_b128 v[52:55], v92 offset:45056
	ds_bpermute_b32 v90, v87, v88
	s_waitcnt lgkmcnt(2)
	v_exp_f32_e32 v114, v114
	v_exp_f32_e32 v115, v115
	v_mfma_f32_32x32x8_f16 v[96:111], v[32:33], v[28:29], 0
	ds_read_u16 v32, v9 offset:224
	ds_read_b128 v[56:59], v92 offset:46080
	v_fmac_f32_e32 v144, v112, v175
	v_exp_f32_e32 v116, v116
	v_fmac_f32_e32 v145, v113, v144
	v_exp_f32_e32 v117, v117
	v_fmac_f32_e32 v146, v114, v145
	v_cvt_pkrtz_f16_f32 v68, v144, v145
	v_exp_f32_e32 v118, v118
	v_fmac_f32_e32 v147, v115, v146
	v_pk_mul_f16 v68, v60, v68
	v_exp_f32_e32 v119, v119
	v_add_f32_e32 v84, v76, v77
	v_add_f32_e32 v91, v78, v79
	v_fmac_f32_e32 v148, v116, v147
	v_add_f32_e32 v84, v84, v91
	v_cvt_pkrtz_f16_f32 v69, v146, v147
	v_mfma_f32_32x32x16_f16 v[128:143], v[36:39], v[44:47], 0
	ds_read_b128 v[44:47], v92 offset:14336
	ds_bpermute_b32 v89, v86, v84
	v_exp_f32_e32 v120, v120
	v_fmac_f32_e32 v149, v117, v148
	v_pk_mul_f16 v69, v61, v69
	v_exp_f32_e32 v121, v121
	v_fmac_f32_e32 v150, v118, v149
	v_cvt_pkrtz_f16_f32 v70, v148, v149
	v_exp_f32_e32 v122, v122
	v_fmac_f32_e32 v151, v119, v150
	v_pk_mul_f16 v70, v62, v70
	v_exp_f32_e32 v123, v123
	v_mfma_f32_32x32x16_f16 v[160:175], v[36:39], v[48:51], 0
	ds_read_b128 v[36:39], v11 offset:1792
	ds_read_b128 v[48:51], v92 offset:15360
	v_cvt_pkrtz_f16_f32 v71, v150, v151
	v_fmac_f32_e32 v184, v120, v151
	v_pk_mul_f16 v71, v63, v71
	v_exp_f32_e32 v124, v124
	v_fmac_f32_e32 v185, v121, v184
	v_mfma_f32_16x16x32_f16 v[80:83], v[68:71], v[20:23], 0
	v_cvt_pkrtz_f16_f32 v72, v184, v185
	v_exp_f32_e32 v125, v125
	v_fmac_f32_e32 v186, v122, v185
	v_pk_mul_f16 v72, v64, v72
	v_fmac_f32_e32 v187, v123, v186
	v_exp_f32_e32 v126, v126
	v_cvt_pkrtz_f16_f32 v73, v186, v187
	v_fmac_f32_e32 v188, v124, v187
	v_pk_mul_f16 v73, v65, v73
	v_fmac_f32_e32 v189, v125, v188
	v_exp_f32_e32 v127, v127
	v_cvt_pkrtz_f16_f32 v74, v188, v189
	v_fmac_f32_e32 v190, v126, v189
	v_pk_mul_f16 v74, v66, v74
	s_waitcnt lgkmcnt(2)
	v_add_f32_e32 v195, v88, v90
	v_fmac_f32_e32 v191, v127, v190
	v_add_f32_e32 v85, v84, v89
	v_cvt_pkrtz_f16_f32 v75, v190, v191
	v_pk_mul_f16 v75, v67, v75
	v_exp_f32_e32 v96, v96
	v_exp_f32_e32 v97, v97
	v_mfma_f32_16x16x32_f16 v[80:83], v[72:75], v[24:27], v[80:83]
	ds_read_b128 v[60:63], v92 offset:47104
	ds_read_b128 v[64:67], v92 offset:48128
	ds_bpermute_b32 v90, v87, v85
	s_waitcnt vmcnt(0)
	ds_write_b16 v94, v18
	ds_write_b16 v94, v19 offset:1024
	s_waitcnt lgkmcnt(0)
	s_barrier
	v_exp_f32_e32 v98, v98
	v_exp_f32_e32 v99, v99
	v_mfma_f32_32x32x8_f16 v[112:127], v[32:33], v[28:29], 0
	s_mov_b32 m0, s32
	ds_read_u16 v32, v10 offset:0
	global_load_lds_dwordx4 v2, s[20:21]
	v_fmac_f32_e32 v128, v96, v191
	v_exp_f32_e32 v100, v100
	v_fmac_f32_e32 v129, v97, v128
	v_exp_f32_e32 v101, v101
	v_fmac_f32_e32 v130, v98, v129
	v_cvt_pkrtz_f16_f32 v68, v128, v129
	v_exp_f32_e32 v102, v102
	v_fmac_f32_e32 v131, v99, v130
	v_pk_mul_f16 v68, v52, v68
	v_exp_f32_e32 v103, v103
	v_add_f32_e32 v84, v80, v81
	v_add_f32_e32 v91, v82, v83
	v_fmac_f32_e32 v132, v100, v131
	v_add_f32_e32 v84, v84, v91
	v_cvt_pkrtz_f16_f32 v69, v130, v131
	v_mfma_f32_32x32x16_f16 v[144:159], v[36:39], v[44:47], 0
	ds_read_b128 v[44:47], v93 offset:0
	ds_bpermute_b32 v89, v86, v84
	s_add_i32 m0, s32, 32768
	s_nop 0
	global_load_lds_dwordx4 v2, s[22:23]
	v_exp_f32_e32 v104, v104
	v_fmac_f32_e32 v133, v101, v132
	v_pk_mul_f16 v69, v53, v69
	v_exp_f32_e32 v105, v105
	v_fmac_f32_e32 v134, v102, v133
	v_cvt_pkrtz_f16_f32 v70, v132, v133
	v_exp_f32_e32 v106, v106
	v_fmac_f32_e32 v135, v103, v134
	v_pk_mul_f16 v70, v54, v70
	v_exp_f32_e32 v107, v107
	v_mfma_f32_32x32x16_f16 v[176:191], v[36:39], v[48:51], 0
	ds_read_b128 v[36:39], v13 offset:0
	s_mov_b32 m0, s33
	ds_read_b128 v[48:51], v93 offset:1024
	global_load_lds_dwordx4 v3, s[20:21]
	v_cvt_pkrtz_f16_f32 v71, v134, v135
	v_fmac_f32_e32 v168, v104, v135
	v_pk_mul_f16 v71, v55, v71
	v_exp_f32_e32 v108, v108
	v_fmac_f32_e32 v169, v105, v168
	v_mfma_f32_16x16x32_f16 v[76:79], v[68:71], v[20:23], 0
	s_add_i32 m0, s33, 32768
	s_nop 0
	global_load_lds_dwordx4 v3, s[22:23]
	v_cvt_pkrtz_f16_f32 v72, v168, v169
	v_exp_f32_e32 v109, v109
	v_fmac_f32_e32 v170, v106, v169
	v_pk_mul_f16 v72, v56, v72
	v_fmac_f32_e32 v171, v107, v170
	v_exp_f32_e32 v110, v110
	v_cvt_pkrtz_f16_f32 v73, v170, v171
	v_fmac_f32_e32 v172, v108, v171
	v_pk_mul_f16 v73, v57, v73
	v_fmac_f32_e32 v173, v109, v172
	v_exp_f32_e32 v111, v111
	v_cvt_pkrtz_f16_f32 v74, v172, v173
	v_fmac_f32_e32 v174, v110, v173
	v_pk_mul_f16 v74, v58, v74
	s_waitcnt lgkmcnt(2)
	v_add_f32_e32 v196, v85, v90
	v_fmac_f32_e32 v175, v111, v174
	v_add_f32_e32 v88, v84, v89
	v_cvt_pkrtz_f16_f32 v75, v174, v175
	v_pk_mul_f16 v75, v59, v75
	v_exp_f32_e32 v112, v112
	v_exp_f32_e32 v113, v113
	v_mfma_f32_16x16x32_f16 v[76:79], v[72:75], v[24:27], v[76:79]
	s_mov_b32 m0, s34
	ds_read_b128 v[52:55], v93 offset:32768
	global_load_lds_dwordx4 v4, s[20:21]
	ds_bpermute_b32 v90, v87, v88
	s_waitcnt lgkmcnt(2)
	v_exp_f32_e32 v114, v114
	v_exp_f32_e32 v115, v115
	v_mfma_f32_32x32x8_f16 v[96:111], v[32:33], v[28:29], 0
	ds_read_u16 v32, v10 offset:32
	s_add_i32 m0, s34, 32768
	ds_read_b128 v[56:59], v93 offset:33792
	global_load_lds_dwordx4 v4, s[22:23]
	v_fmac_f32_e32 v144, v112, v175
	v_exp_f32_e32 v116, v116
	v_fmac_f32_e32 v145, v113, v144
	v_exp_f32_e32 v117, v117
	v_fmac_f32_e32 v146, v114, v145
	v_cvt_pkrtz_f16_f32 v68, v144, v145
	v_exp_f32_e32 v118, v118
	v_fmac_f32_e32 v147, v115, v146
	v_pk_mul_f16 v68, v60, v68
	v_exp_f32_e32 v119, v119
	v_add_f32_e32 v84, v76, v77
	v_add_f32_e32 v91, v78, v79
	v_fmac_f32_e32 v148, v116, v147
	v_add_f32_e32 v84, v84, v91
	v_cvt_pkrtz_f16_f32 v69, v146, v147
	v_mfma_f32_32x32x16_f16 v[128:143], v[36:39], v[44:47], 0
	ds_read_b128 v[44:47], v93 offset:2048
	ds_bpermute_b32 v89, v86, v84
	s_cmp_eq_u32 s40, 0
	s_cselect_b64 s[56:57], 0, s[42:43]
	s_and_saveexec_b64 s[44:45], s[56:57]
	global_store_dword v[16:17], v197, off offset:-192
	global_store_dword v[16:17], v198, off offset:-128
	global_store_dword v[16:17], v199, off offset:-64
	s_and_b64 exec, s[44:45], s[42:43]
	global_store_dword v[16:17], v192, off
	global_store_dword v[16:17], v193, off offset:64
	global_store_dword v[16:17], v194, off offset:128
	global_store_dword v[16:17], v195, off offset:192
	global_store_dword v[16:17], v196, off offset:256
	s_mov_b64 exec, s[44:45]
	v_exp_f32_e32 v120, v120
	v_fmac_f32_e32 v149, v117, v148
	v_pk_mul_f16 v69, v61, v69
	v_exp_f32_e32 v121, v121
	v_fmac_f32_e32 v150, v118, v149
	v_cvt_pkrtz_f16_f32 v70, v148, v149
	v_exp_f32_e32 v122, v122
	v_fmac_f32_e32 v151, v119, v150
	v_pk_mul_f16 v70, v62, v70
	v_exp_f32_e32 v123, v123
	v_mfma_f32_32x32x16_f16 v[160:175], v[36:39], v[48:51], 0
	ds_read_b128 v[36:39], v13 offset:256
	s_mov_b32 m0, s35
	ds_read_b128 v[48:51], v93 offset:3072
	global_load_lds_dwordx4 v5, s[20:21]
	s_add_i32 m0, s35, 32768
	s_nop 0
	global_load_lds_dwordx4 v5, s[22:23]
	v_cvt_pkrtz_f16_f32 v71, v150, v151
	v_fmac_f32_e32 v184, v120, v151
	v_pk_mul_f16 v71, v63, v71
	v_exp_f32_e32 v124, v124
	v_fmac_f32_e32 v185, v121, v184
	v_mfma_f32_16x16x32_f16 v[80:83], v[68:71], v[20:23], 0
	s_mov_b32 m0, s29
	s_nop 0
	global_load_lds_dword v6, s[24:25]
	global_load_ushort v18, v7, s[26:27]
	global_load_ushort v19, v7, s[26:27] offset:128
	v_cvt_pkrtz_f16_f32 v72, v184, v185
	v_exp_f32_e32 v125, v125
	v_fmac_f32_e32 v186, v122, v185
	v_pk_mul_f16 v72, v64, v72
	v_fmac_f32_e32 v187, v123, v186
	v_exp_f32_e32 v126, v126
	v_cvt_pkrtz_f16_f32 v73, v186, v187
	v_fmac_f32_e32 v188, v124, v187
	v_pk_mul_f16 v73, v65, v73
	v_fmac_f32_e32 v189, v125, v188
	v_exp_f32_e32 v127, v127
	v_cvt_pkrtz_f16_f32 v74, v188, v189
	v_fmac_f32_e32 v190, v126, v189
	v_pk_mul_f16 v74, v66, v74
	s_waitcnt lgkmcnt(2)
	v_add_f32_e32 v197, v88, v90
	v_fmac_f32_e32 v191, v127, v190
	v_add_f32_e32 v85, v84, v89
	v_cvt_pkrtz_f16_f32 v75, v190, v191
	s_cmp_lt_u32 s40, 29
	s_cselect_b32 s58, 0x4000, 0
	s_cselect_b32 s59, 0x100, 0
	s_add_u32 s20, s20, s58
	s_addc_u32 s21, s21, 0
	s_add_u32 s22, s22, s58
	s_addc_u32 s23, s23, 0
	s_add_u32 s24, s24, s59
	s_addc_u32 s25, s25, 0
	s_add_u32 s26, s26, s59
	s_addc_u32 s27, s27, 0
	v_pk_mul_f16 v75, v67, v75
	v_lshl_add_u64 v[16:17], v[16:17], 0, s[46:47]
	v_swap_b32 v92, v93
	v_swap_b32 v9, v10
	v_swap_b32 v11, v13
	v_swap_b32 v8, v94
	s_xor_b32 s32, s32, 0x4000
	s_xor_b32 s33, s33, 0x4000
	s_xor_b32 s34, s34, 0x4000
	s_xor_b32 s35, s35, 0x4000
	s_xor_b32 s29, s29, 0x100
	s_add_u32 s40, s40, 1
	s_cmp_lt_u32 s40, 32
	s_cbranch_scc1 .Lscan_loop
	s_nop 1
	v_mfma_f32_16x16x32_f16 v[80:83], v[72:75], v[24:27], v[80:83]
	ds_bpermute_b32 v90, v87, v85
	s_nop 15
	v_add_f32_e32 v84, v80, v81
	v_add_f32_e32 v91, v82, v83
	s_nop 0
	v_add_f32_e32 v84, v84, v91
	s_waitcnt lgkmcnt(0)
	v_add_f32_e32 v198, v85, v90
	ds_bpermute_b32 v89, v86, v84
	s_waitcnt lgkmcnt(0)
	v_add_f32_e32 v88, v84, v89
	s_nop 0
	ds_bpermute_b32 v90, v87, v88
	s_waitcnt lgkmcnt(0)
	v_add_f32_e32 v199, v88, v90
	s_nop 1
	s_and_saveexec_b64 s[44:45], s[42:43]
	global_store_dword v[16:17], v197, off offset:-192
	global_store_dword v[16:17], v198, off offset:-128
	global_store_dword v[16:17], v199, off offset:-64
	s_waitcnt vmcnt(0)
	s_endpgm

_Z9deconv3_kPKDF16_PKfS2_Pf:
	s_load_dwordx4 s[8:11], s[0:1], 0x0
	s_load_dwordx4 s[12:15], s[0:1], 0x10
	v_lshlrev_b32_e32 v1, 2, v0
	v_and_b32_e32 v2, 7, v0
	v_lshrrev_b32_e32 v3, 3, v0
	s_lshl_b32 s20, s2, 5
	v_add_u32_e32 v3, s20, v3
	v_and_b32_e32 v4, 63, v3
	v_bfe_u32 v5, v3, 6, 6
	v_and_b32_e32 v6, 0xfffff000, v3
	v_lshlrev_b32_e32 v58, 4, v2
	v_mov_b32_e32 v7, 0
	s_waitcnt lgkmcnt(0)
	s_load_dwordx2 s[16:17], s[12:13], 0x0
	s_load_dword s18, s[12:13], 0x8
	v_add_u32_e32 v17, 0, v0
	v_mul_u32_u24_e32 v18, 0x2ab, v17
	v_lshrrev_b32_e32 v18, 17, v18
	v_mul_u32_u24_e32 v19, 0xc0, v18
	v_sub_u32_e32 v19, v17, v19
	v_mul_u32_u24_e32 v19, 9, v19
	v_sub_u32_e32 v19, v19, v18
	v_add_u32_e32 v19, 8, v19
	v_lshlrev_b32_e32 v19, 2, v19
	global_load_dword v10, v19, s[10:11]
	v_add_u32_e32 v17, 256, v0
	v_mul_u32_u24_e32 v18, 0x2ab, v17
	v_lshrrev_b32_e32 v18, 17, v18
	v_mul_u32_u24_e32 v19, 0xc0, v18
	v_sub_u32_e32 v19, v17, v19
	v_mul_u32_u24_e32 v19, 9, v19
	v_sub_u32_e32 v19, v19, v18
	v_add_u32_e32 v19, 8, v19
	v_lshlrev_b32_e32 v19, 2, v19
	global_load_dword v11, v19, s[10:11]
	v_add_u32_e32 v17, 512, v0
	v_mul_u32_u24_e32 v18, 0x2ab, v17
	v_lshrrev_b32_e32 v18, 17, v18
	v_mul_u32_u24_e32 v19, 0xc0, v18
	v_sub_u32_e32 v19, v17, v19
	v_mul_u32_u24_e32 v19, 9, v19
	v_sub_u32_e32 v19, v19, v18
	v_add_u32_e32 v19, 8, v19
	v_lshlrev_b32_e32 v19, 2, v19
	global_load_dword v12, v19, s[10:11]
	v_add_u32_e32 v17, 768, v0
	v_mul_u32_u24_e32 v18, 0x2ab, v17
	v_lshrrev_b32_e32 v18, 17, v18
	v_mul_u32_u24_e32 v19, 0xc0, v18
	v_sub_u32_e32 v19, v17, v19
	v_mul_u32_u24_e32 v19, 9, v19
	v_sub_u32_e32 v19, v19, v18
	v_add_u32_e32 v19, 8, v19
	v_lshlrev_b32_e32 v19, 2, v19
	global_load_dword v13, v19, s[10:11]
	v_add_u32_e32 v17, 1024, v0
	v_mul_u32_u24_e32 v18, 0x2ab, v17
	v_lshrrev_b32_e32 v18, 17, v18
	v_mul_u32_u24_e32 v19, 0xc0, v18
	v_sub_u32_e32 v19, v17, v19
	v_mul_u32_u24_e32 v19, 9, v19
	v_sub_u32_e32 v19, v19, v18
	v_add_u32_e32 v19, 8, v19
	v_lshlrev_b32_e32 v19, 2, v19
	global_load_dword v14, v19, s[10:11]
	v_add_u32_e32 v17, 1280, v0
	v_mul_u32_u24_e32 v18, 0x2ab, v17
	v_lshrrev_b32_e32 v18, 17, v18
	v_mul_u32_u24_e32 v19, 0xc0, v18
	v_sub_u32_e32 v19, v17, v19
	v_mul_u32_u24_e32 v19, 9, v19
	v_sub_u32_e32 v19, v19, v18
	v_add_u32_e32 v19, 8, v19
	v_lshlrev_b32_e32 v19, 2, v19
	global_load_dword v15, v19, s[10:11]
	v_add_u32_e32 v17, 1536, v0
	v_mul_u32_u24_e32 v18, 0x2ab, v17
	v_lshrrev_b32_e32 v18, 17, v18
	v_mul_u32_u24_e32 v19, 0xc0, v18
	v_sub_u32_e32 v19, v17, v19
	v_mul_u32_u24_e32 v19, 9, v19
	v_sub_u32_e32 v19, v19, v18
	v_add_u32_e32 v19, 8, v19
	v_lshlrev_b32_e32 v19, 2, v19
	v_cmp_gt_u32_e32 vcc, 0xc0, v0
	s_and_saveexec_b64 s[22:23], vcc
	global_load_dword v16, v19, s[10:11]
	s_mov_b64 exec, s[22:23]
	v_add_u32_e32 v17, -1, v5
	v_add_u32_e32 v18, -1, v4
	v_max_u32_e32 v19, v17, v18
	v_cmp_gt_u32_e32 vcc, 64, v19
	v_lshl_add_u32 v17, v17, 6, v18
	v_add_u32_e32 v17, v6, v17
	v_cndmask_b32_e32 v17, v3, v17, vcc
	v_cndmask_b32_e64 v18, 0, 1, vcc
	v_lshl_or_b32 v7, v18, 0, v7
	v_lshl_add_u32 v17, v17, 7, v58
	global_load_dwordx4 v[20:23], v17, s[8:9]
	v_add_u32_e32 v17, -1, v5
	v_add_u32_e32 v18, 0, v4
	v_max_u32_e32 v19, v17, v18
	v_cmp_gt_u32_e32 vcc, 64, v19
	v_lshl_add_u32 v17, v17, 6, v18
	v_add_u32_e32 v17, v6, v17
	v_cndmask_b32_e32 v17, v3, v17, vcc
	v_cndmask_b32_e64 v18, 0, 1, vcc
	v_lshl_or_b32 v7, v18, 1, v7
	v_lshl_add_u32 v17, v17, 7, v58
	global_load_dwordx4 v[24:27], v17, s[8:9]
	v_add_u32_e32 v17, -1, v5
	v_add_u32_e32 v18, 1, v4
	v_max_u32_e32 v19, v17, v18
	v_cmp_gt_u32_e32 vcc, 64, v19
	v_lshl_add_u32 v17, v17, 6, v18
	v_add_u32_e32 v17, v6, v17
	v_cndmask_b32_e32 v17, v3, v17, vcc
	v_cndmask_b32_e64 v18, 0, 1, vcc
	v_lshl_or_b32 v7, v18, 2, v7
	v_lshl_add_u32 v17, v17, 7, v58
	global_load_dwordx4 v[28:31], v17, s[8:9]
	v_add_u32_e32 v17, 0, v5
	v_add_u32_e32 v18, -1, v4
	v_max_u32_e32 v19, v17, v18
	v_cmp_gt_u32_e32 vcc, 64, v19
	v_lshl_add_u32 v17, v17, 6, v18
	v_add_u32_e32 v17, v6, v17
	v_cndmask_b32_e32 v17, v3, v17, vcc
	v_cndmask_b32_e64 v18, 0, 1, vcc
	v_lshl_or_b32 v7, v18, 3, v7
	v_lshl_add_u32 v17, v17, 7, v58
	global_load_dwordx4 v[32:35], v17, s[8:9]
	v_add_u32_e32 v17, 0, v5
	v_add_u32_e32 v18, 0, v4
	v_max_u32_e32 v19, v17, v18
	v_cmp_gt_u32_e32 vcc, 64, v19
	v_lshl_add_u32 v17, v17, 6, v18
	v_add_u32_e32 v17, v6, v17
	v_cndmask_b32_e32 v17, v3, v17, vcc
	v_cndmask_b32_e64 v18, 0, 1, vcc
	v_lshl_or_b32 v7, v18, 4, v7
	v_lshl_add_u32 v17, v17, 7, v58
	global_load_dwordx4 v[36:39], v17, s[8:9]
	v_add_u32_e32 v17, 0, v5
	v_add_u32_e32 v18, 1, v4
	v_max_u32_e32 v19, v17, v18
	v_cmp_gt_u32_e32 vcc, 64, v19
	v_lshl_add_u32 v17, v17, 6, v18
	v_add_u32_e32 v17, v6, v17
	v_cndmask_b32_e32 v17, v3, v17, vcc
	v_cndmask_b32_e64 v18, 0, 1, vcc
	v_lshl_or_b32 v7, v18, 5, v7
	v_lshl_add_u32 v17, v17, 7, v58
	global_load_dwordx4 v[40:43], v17, s[8:9]
	v_add_u32_e32 v17, 1, v5
	v_add_u32_e32 v18, -1, v4
	v_max_u32_e32 v19, v17, v18
	v_cmp_gt_u32_e32 vcc, 64, v19
	v_lshl_add_u32 v17, v17, 6, v18
	v_add_u32_e32 v17, v6, v17
	v_cndmask_b32_e32 v17, v3, v17, vcc
	v_cndmask_b32_e64 v18, 0, 1, vcc
	v_lshl_or_b32 v7, v18, 6, v7
	v_lshl_add_u32 v17, v17, 7, v58
	global_load_dwordx4 v[44:47], v17, s[8:9]
	v_add_u32_e32 v17, 1, v5
	v_add_u32_e32 v18, 0, v4
	v_max_u32_e32 v19, v17, v18
	v_cmp_gt_u32_e32 vcc, 64, v19
	v_lshl_add_u32 v17, v17, 6, v18
	v_add_u32_e32 v17, v6, v17
	v_cndmask_b32_e32 v17, v3, v17, vcc
	v_cndmask_b32_e64 v18, 0, 1, vcc
	v_lshl_or_b32 v7, v18, 7, v7
	v_lshl_add_u32 v17, v17, 7, v58
	global_load_dwordx4 v[48:51], v17, s[8:9]
	v_add_u32_e32 v17, 1, v5
	v_add_u32_e32 v18, 1, v4
	v_max_u32_e32 v19, v17, v18
	v_cmp_gt_u32_e32 vcc, 64, v19
	v_lshl_add_u32 v17, v17, 6, v18
	v_add_u32_e32 v17, v6, v17
	v_cndmask_b32_e32 v17, v3, v17, vcc
	v_cndmask_b32_e64 v18, 0, 1, vcc
	v_lshl_or_b32 v7, v18, 8, v7
	v_lshl_add_u32 v17, v17, 7, v58
	global_load_dwordx4 v[52:55], v17, s[8:9]
	s_waitcnt vmcnt(9)
	ds_write_b32 v1, v10
	ds_write_b32 v1, v11 offset:1024
	ds_write_b32 v1, v12 offset:2048
	ds_write_b32 v1, v13 offset:3072
	ds_write_b32 v1, v14 offset:4096
	ds_write_b32 v1, v15 offset:5120
	v_cmp_gt_u32_e32 vcc, 0xc0, v0
	s_and_saveexec_b64 s[22:23], vcc
	ds_write_b32 v1, v16 offset:6144
	s_mov_b64 exec, s[22:23]
	v_lshlrev_b32_e32 v8, 4, v0
	v_add_u32_e32 v8, 6912, v8
	s_waitcnt vmcnt(8)
	ds_write_b128 v8, v[20:23] offset:0
	s_waitcnt vmcnt(7)
	ds_write_b128 v8, v[24:27] offset:4096
	s_waitcnt vmcnt(6)
	ds_write_b128 v8, v[28:31] offset:8192
	s_waitcnt vmcnt(5)
	ds_write_b128 v8, v[32:35] offset:12288
	s_waitcnt vmcnt(4)
	ds_write_b128 v8, v[36:39] offset:16384
	s_waitcnt vmcnt(3)
	ds_write_b128 v8, v[40:43] offset:20480
	s_waitcnt vmcnt(2)
	ds_write_b128 v8, v[44:47] offset:24576
	s_waitcnt vmcnt(1)
	ds_write_b128 v8, v[48:51] offset:28672
	s_waitcnt vmcnt(0)
	ds_write_b128 v8, v[52:55] offset:32768
	v_mul_u32_u24_e32 v9, 96, v2
	v_mov_b32_e32 v48, 0
	v_mov_b32_e32 v49, 0
	v_mov_b32_e32 v50, 0
	s_mov_b32 s21, 0
	s_waitcnt lgkmcnt(0)
	s_barrier
.Ldc3_tap:
	ds_read_b128 v[20:23], v8
	ds_read_b128 v[24:27], v9
	ds_read_b128 v[28:31], v9 offset:16
	ds_read_b128 v[32:35], v9 offset:32
	ds_read_b128 v[36:39], v9 offset:48
	ds_read_b128 v[40:43], v9 offset:64
	ds_read_b128 v[44:47], v9 offset:80
	v_bfe_i32 v56, v7, s21, 1
	s_waitcnt lgkmcnt(6)
	v_and_b32_e32 v20, v56, v20
	v_and_b32_e32 v21, v56, v21
	v_and_b32_e32 v22, v56, v22
	v_and_b32_e32 v23, v56, v23
	s_waitcnt lgkmcnt(0)
	v_fma_mix_f32 v48, v24, v20, v48 op_sel_hi:[0,1,0]
	v_fma_mix_f32 v49, v25, v20, v49 op_sel_hi:[0,1,0]
	v_fma_mix_f32 v50, v26, v20, v50 op_sel_hi:[0,1,0]
	v_fma_mix_f32 v48, v27, v20, v48 op_sel:[0,1,0] op_sel_hi:[0,1,0]
	v_fma_mix_f32 v49, v28, v20, v49 op_sel:[0,1,0] op_sel_hi:[0,1,0]
	v_fma_mix_f32 v50, v29, v20, v50 op_sel:[0,1,0] op_sel_hi:[0,1,0]
	v_fma_mix_f32 v48, v30, v21, v48 op_sel_hi:[0,1,0]
	v_fma_mix_f32 v49, v31, v21, v49 op_sel_hi:[0,1,0]
	v_fma_mix_f32 v50, v32, v21, v50 op_sel_hi:[0,1,0]
	v_fma_mix_f32 v48, v33, v21, v48 op_sel:[0,1,0] op_sel_hi:[0,1,0]
	v_fma_mix_f32 v49, v34, v21, v49 op_sel:[0,1,0] op_sel_hi:[0,1,0]
	v_fma_mix_f32 v50, v35, v21, v50 op_sel:[0,1,0] op_sel_hi:[0,1,0]
	v_fma_mix_f32 v48, v36, v22, v48 op_sel_hi:[0,1,0]
	v_fma_mix_f32 v49, v37, v22, v49 op_sel_hi:[0,1,0]
	v_fma_mix_f32 v50, v38, v22, v50 op_sel_hi:[0,1,0]
	v_fma_mix_f32 v48, v39, v22, v48 op_sel:[0,1,0] op_sel_hi:[0,1,0]
	v_fma_mix_f32 v49, v40, v22, v49 op_sel:[0,1,0] op_sel_hi:[0,1,0]
	v_fma_mix_f32 v50, v41, v22, v50 op_sel:[0,1,0] op_sel_hi:[0,1,0]
	v_fma_mix_f32 v48, v42, v23, v48 op_sel_hi:[0,1,0]
	v_fma_mix_f32 v49, v43, v23, v49 op_sel_hi:[0,1,0]
	v_fma_mix_f32 v50, v44, v23, v50 op_sel_hi:[0,1,0]
	v_fma_mix_f32 v48, v45, v23, v48 op_sel:[0,1,0] op_sel_hi:[0,1,0]
	v_fma_mix_f32 v49, v46, v23, v49 op_sel:[0,1,0] op_sel_hi:[0,1,0]
	v_fma_mix_f32 v50, v47, v23, v50 op_sel:[0,1,0] op_sel_hi:[0,1,0]
	v_add_u32_e32 v8, 0x1000, v8
	v_add_u32_e32 v9, 0x300, v9
	s_add_u32 s21, s21, 1
	s_cmp_lt_u32 s21, 9
	s_cbranch_scc1 .Ldc3_tap
	s_nop 1
	v_add_f32_dpp v48, v48, v48 quad_perm:[1,0,3,2] row_mask:0xf bank_mask:0xf
	v_add_f32_dpp v49, v49, v49 quad_perm:[1,0,3,2] row_mask:0xf bank_mask:0xf
	v_add_f32_dpp v50, v50, v50 quad_perm:[1,0,3,2] row_mask:0xf bank_mask:0xf
	v_add_f32_dpp v48, v48, v48 quad_perm:[2,3,0,1] row_mask:0xf bank_mask:0xf
	v_add_f32_dpp v49, v49, v49 quad_perm:[2,3,0,1] row_mask:0xf bank_mask:0xf
	v_add_f32_dpp v50, v50, v50 quad_perm:[2,3,0,1] row_mask:0xf bank_mask:0xf
	v_add_f32_dpp v48, v48, v48 row_half_mirror row_mask:0xf bank_mask:0xf
	v_add_f32_dpp v49, v49, v49 row_half_mirror row_mask:0xf bank_mask:0xf
	v_add_f32_dpp v50, v50, v50 row_half_mirror row_mask:0xf bank_mask:0xf
	v_lshrrev_b32_e32 v17, 12, v3
	v_mul_u32_u24_e32 v17, 0x3000, v17
	v_and_b32_e32 v18, 0xfff, v3
	v_add_u32_e32 v17, v17, v18
	v_lshlrev_b32_e32 v17, 2, v17
	v_add_u32_e32 v18, 0x4000, v17
	v_add_u32_e32 v19, 0x8000, v17
	v_add_f32_e32 v48, s16, v48
	v_add_f32_e32 v49, s17, v49
	v_add_f32_e32 v50, s18, v50
	v_max_f32_e32 v48, 0, v48
	v_max_f32_e32 v49, 0, v49
	v_max_f32_e32 v50, 0, v50
	v_cmp_eq_u32_e32 vcc, 0, v2
	s_and_saveexec_b64 s[22:23], vcc
	global_store_dword v17, v48, s[14:15]
	global_store_dword v18, v49, s[14:15]
	global_store_dword v19, v50, s[14:15]
	s_endpgm

	.amdhsa_kernel _Z9deconv3_kPKDF16_PKfS2_Pf
		.amdhsa_group_segment_fixed_size 43776
		.amdhsa_private_segment_fixed_size 0
		.amdhsa_kernarg_size 32
		.amdhsa_user_sgpr_count 2
		.amdhsa_user_sgpr_dispatch_ptr 0
		.amdhsa_user_sgpr_queue_ptr 0
		.amdhsa_user_sgpr_kernarg_segment_ptr 1
		.amdhsa_user_sgpr_dispatch_id 0
		.amdhsa_user_sgpr_kernarg_preload_length 0
		.amdhsa_user_sgpr_kernarg_preload_offset 0
		.amdhsa_user_sgpr_private_segment_size 0
		.amdhsa_uses_dynamic_stack 0
		.amdhsa_enable_private_segment 0
		.amdhsa_system_sgpr_workgroup_id_x 1
		.amdhsa_system_sgpr_workgroup_id_y 0
		.amdhsa_system_sgpr_workgroup_id_z 0
		.amdhsa_system_sgpr_workgroup_info 0
		.amdhsa_system_vgpr_workitem_id 0
		.amdhsa_next_free_vgpr 60
		.amdhsa_next_free_sgpr 24
		.amdhsa_accum_offset 60
		.amdhsa_reserve_vcc 1
		.amdhsa_float_round_mode_32 0
		.amdhsa_float_round_mode_16_64 0
		.amdhsa_float_denorm_mode_32 3
		.amdhsa_float_denorm_mode_16_64 3
		.amdhsa_dx10_clamp 1
		.amdhsa_ieee_mode 1
		.amdhsa_fp16_overflow 0
		.amdhsa_tg_split 0
		.amdhsa_exception_fp_ieee_invalid_op 0
		.amdhsa_exception_fp_denorm_src 0
		.amdhsa_exception_fp_ieee_div_zero 0
		.amdhsa_exception_fp_ieee_overflow 0
		.amdhsa_exception_fp_ieee_underflow 0
		.amdhsa_exception_fp_ieee_inexact 0
		.amdhsa_exception_int_div_zero 0
	.end_amdhsa_kernel

amdhsa.kernels:
  - .agpr_count:     0
    .args:
      - .offset:         0
        .size:           152
        .value_kind:     by_value
    .group_segment_fixed_size: 7168
    .kernarg_segment_align: 8
    .kernarg_segment_size: 152
    .language:       OpenCL C
    .language_version:
      - 2
      - 0
    .max_flat_workgroup_size: 256
    .name:           _Z6prep_k5PrepP
    .private_segment_fixed_size: 0
    .sgpr_count:     70
    .sgpr_spill_count: 0
    .symbol:         _Z6prep_k5PrepP.kd
    .uniform_work_group_size: 1
    .uses_dynamic_stack: false
    .vgpr_count:     64
    .vgpr_spill_count: 0
    .wavefront_size: 64
  - .agpr_count:     0
    .args:
      - .actual_access:  read_only
        .address_space:  global
        .offset:         0
        .size:           8
        .value_kind:     global_buffer
      - .actual_access:  read_only
        .address_space:  global
        .offset:         8
        .size:           8
        .value_kind:     global_buffer
      - .actual_access:  read_only
        .address_space:  global
        .offset:         16
        .size:           8
        .value_kind:     global_buffer
      - .actual_access:  write_only
        .address_space:  global
        .offset:         24
        .size:           8
        .value_kind:     global_buffer
      - .actual_access:  write_only
        .address_space:  global
        .offset:         32
        .size:           8
        .value_kind:     global_buffer
    .group_segment_fixed_size: 9216
    .kernarg_segment_align: 8
    .kernarg_segment_size: 40
    .language:       OpenCL C
    .language_version:
      - 2
      - 0
    .max_flat_workgroup_size: 256
    .name:           _Z8conv1d_kPKDF16_PKfS2_PDF16_S3_
    .private_segment_fixed_size: 0
    .sgpr_count:     22
    .sgpr_spill_count: 0
    .symbol:         _Z8conv1d_kPKDF16_PKfS2_PDF16_S3_.kd
    .uniform_work_group_size: 1
    .uses_dynamic_stack: false
    .vgpr_count:     53
    .vgpr_spill_count: 0
    .wavefront_size: 64
  - .agpr_count:     0
    .args:
      - .actual_access:  read_only
        .address_space:  global
        .offset:         0
        .size:           8
        .value_kind:     global_buffer
      - .actual_access:  read_only
        .address_space:  global
        .offset:         8
        .size:           8
        .value_kind:     global_buffer
      - .actual_access:  read_only
        .address_space:  global
        .offset:         16
        .size:           8
        .value_kind:     global_buffer
      - .actual_access:  read_only
        .address_space:  global
        .offset:         24
        .size:           8
        .value_kind:     global_buffer
      - .actual_access:  write_only
        .address_space:  global
        .offset:         32
        .size:           8
        .value_kind:     global_buffer
      - .actual_access:  write_only
        .address_space:  global
        .offset:         40
        .size:           8
        .value_kind:     global_buffer
    .group_segment_fixed_size: 70656
    .kernarg_segment_align: 8
    .kernarg_segment_size: 48
    .language:       OpenCL C
    .language_version:
      - 2
      - 0
    .max_flat_workgroup_size: 256
    .name:           _Z4dt_kPKfS0_S0_PKDF16_PDF16_S3_
    .private_segment_fixed_size: 0
    .sgpr_count:     25
    .sgpr_spill_count: 0
    .symbol:         _Z4dt_kPKfS0_S0_PKDF16_PDF16_S3_.kd
    .uniform_work_group_size: 1
    .uses_dynamic_stack: false
    .vgpr_count:     96
    .vgpr_spill_count: 0
    .wavefront_size: 64
  - .agpr_count:     0
    .args:
      - .address_space:  global
        .offset:         0
        .size:           8
        .value_kind:     global_buffer
      - .actual_access:  read_only
        .address_space:  global
        .offset:         8
        .size:           8
        .value_kind:     global_buffer
      - .address_space:  global
        .offset:         16
        .size:           8
        .value_kind:     global_buffer
      - .address_space:  global
        .offset:         24
        .size:           8
        .value_kind:     global_buffer
      - .actual_access:  read_only
        .address_space:  global
        .offset:         32
        .size:           8
        .value_kind:     global_buffer
      - .actual_access:  write_only
        .address_space:  global
        .offset:         40
        .size:           8
        .value_kind:     global_buffer
    .group_segment_fixed_size: 86016
    .kernarg_segment_align: 8
    .kernarg_segment_size: 48
    .language:       OpenCL C
    .language_version:
      - 2
      - 0
    .max_flat_workgroup_size: 256
    .name:           _Z6scan_kPKDF16_S0_S0_S0_PKfPf
    .private_segment_fixed_size: 0
    .sgpr_count:     66
    .sgpr_spill_count: 0
    .symbol:         _Z6scan_kPKDF16_S0_S0_S0_PKfPf.kd
    .uniform_work_group_size: 1
    .uses_dynamic_stack: false
    .vgpr_count:     200
    .vgpr_spill_count: 0
    .wavefront_size: 64
  - .agpr_count:     0
    .args:
      - .actual_access:  read_only
        .address_space:  global
        .offset:         0
        .size:           8
        .value_kind:     global_buffer
      - .actual_access:  read_only
        .address_space:  global
        .offset:         8
        .size:           8
        .value_kind:     global_buffer
      - .actual_access:  read_only
        .address_space:  global
        .offset:         16
        .size:           8
        .value_kind:     global_buffer
      - .actual_access:  read_only
        .address_space:  global
        .offset:         24
        .size:           8
        .value_kind:     global_buffer
      - .actual_access:  write_only
        .address_space:  global
        .offset:         32
        .size:           8
        .value_kind:     global_buffer
    .group_segment_fixed_size: 9216
    .kernarg_segment_align: 8
    .kernarg_segment_size: 40
    .language:       OpenCL C
    .language_version:
      - 2
      - 0
    .max_flat_workgroup_size: 256
    .name:           _Z6gate_kPKfPKDF16_S2_S0_PDF16_
    .private_segment_fixed_size: 0
    .sgpr_count:     22
    .sgpr_spill_count: 0
    .symbol:         _Z6gate_kPKfPKDF16_S2_S0_PDF16_.kd
    .uniform_work_group_size: 1
    .uses_dynamic_stack: false
    .vgpr_count:     46
    .vgpr_spill_count: 0
    .wavefront_size: 64
  - .agpr_count:     0
    .args:
      - .actual_access:  read_only
        .address_space:  global
        .offset:         0
        .size:           8
        .value_kind:     global_buffer
      - .actual_access:  read_only
        .address_space:  global
        .offset:         8
        .size:           8
        .value_kind:     global_buffer
      - .actual_access:  read_only
        .address_space:  global
        .offset:         16
        .size:           8
        .value_kind:     global_buffer
      - .actual_access:  write_only
        .address_space:  global
        .offset:         24
        .size:           8
        .value_kind:     global_buffer
    .group_segment_fixed_size: 43776
    .kernarg_segment_align: 8
    .kernarg_segment_size: 32
    .language:       OpenCL C
    .language_version:
      - 2
      - 0
    .max_flat_workgroup_size: 256
    .name:           _Z9deconv3_kPKDF16_PKfS2_Pf
    .private_segment_fixed_size: 0
    .sgpr_count:     30
    .sgpr_spill_count: 0
    .symbol:         _Z9deconv3_kPKDF16_PKfS2_Pf.kd
    .uniform_work_group_size: 1
    .uses_dynamic_stack: false
    .vgpr_count:     60
    .vgpr_spill_count: 0
    .wavefront_size: 64
  - .agpr_count:     8
    .args:
      - .offset:         0
        .size:           112
        .value_kind:     by_value
    .group_segment_fixed_size: 49152
    .kernarg_segment_align: 8
    .kernarg_segment_size: 112
    .language:       OpenCL C
    .language_version:
      - 2
      - 0
    .max_flat_workgroup_size: 256
    .name:           _Z6gemm_gILi32ELi64ELi16ELi32ELi1ELi0ELi64ELi4EEv5GemmP
    .private_segment_fixed_size: 0
    .sgpr_count:     34
    .sgpr_spill_count: 0
    .symbol:         _Z6gemm_gILi32ELi64ELi16ELi32ELi1ELi0ELi64ELi4EEv5GemmP.kd
    .uniform_work_group_size: 1
    .uses_dynamic_stack: false
    .vgpr_count:     40
    .vgpr_spill_count: 0
    .wavefront_size: 64
  - .agpr_count:     16
    .args:
      - .offset:         0
        .size:           112
        .value_kind:     by_value
    .group_segment_fixed_size: 65536
    .kernarg_segment_align: 8
    .kernarg_segment_size: 112
    .language:       OpenCL C
    .language_version:
      - 2
      - 0
    .max_flat_workgroup_size: 256
    .name:           _Z6gemm_gILi64ELi64ELi32ELi32ELi1ELi0ELi64ELi4EEv5GemmP
    .private_segment_fixed_size: 0
    .sgpr_count:     34
    .sgpr_spill_count: 0
    .symbol:         _Z6gemm_gILi64ELi64ELi32ELi32ELi1ELi0ELi64ELi4EEv5GemmP.kd
    .uniform_work_group_size: 1
    .uses_dynamic_stack: false
    .vgpr_count:     56
    .vgpr_spill_count: 0
    .wavefront_size: 64
  - .agpr_count:     32
    .args:
      - .offset:         0
        .size:           112
        .value_kind:     by_value
    .group_segment_fixed_size: 73728
    .kernarg_segment_align: 8
    .kernarg_segment_size: 112
    .language:       OpenCL C
    .language_version:
      - 2
      - 0
    .max_flat_workgroup_size: 256
    .name:           _Z6gemm_gILi64ELi128ELi32ELi64ELi0ELi2ELi64ELi3EEv5GemmP
    .private_segment_fixed_size: 0
    .sgpr_count:     27
    .sgpr_spill_count: 0
    .symbol:         _Z6gemm_gILi64ELi128ELi32ELi64ELi0ELi2ELi64ELi3EEv5GemmP.kd
    .uniform_work_group_size: 1
    .uses_dynamic_stack: false
    .vgpr_count:     80
    .vgpr_spill_count: 0
    .wavefront_size: 64
  - .agpr_count:     16
    .args:
      - .offset:         0
        .size:           112
        .value_kind:     by_value
    .group_segment_fixed_size: 49152
    .kernarg_segment_align: 8
    .kernarg_segment_size: 112
    .language:       OpenCL C
    .language_version:
      - 2
      - 0
    .max_flat_workgroup_size: 256
    .name:           _Z6gemm_gILi64ELi64ELi32ELi32ELi0ELi3ELi64ELi3EEv5GemmP
    .private_segment_fixed_size: 0
    .sgpr_count:     30
    .sgpr_spill_count: 0
    .symbol:         _Z6gemm_gILi64ELi64ELi32ELi32ELi0ELi3ELi64ELi3EEv5GemmP.kd
    .uniform_work_group_size: 1
    .uses_dynamic_stack: false
    .vgpr_count:     56
    .vgpr_spill_count: 0
    .wavefront_size: 64
  - .agpr_count:     16
    .args:
      - .offset:         0
        .size:           112
        .value_kind:     by_value
    .group_segment_fixed_size: 49152
    .kernarg_segment_align: 8
    .kernarg_segment_size: 112
    .language:       OpenCL C
    .language_version:
      - 2
      - 0
    .max_flat_workgroup_size: 256
    .name:           _Z6gemm_gILi64ELi64ELi32ELi32ELi0ELi4ELi64ELi3EEv5GemmP
    .private_segment_fixed_size: 0
    .sgpr_count:     27
    .sgpr_spill_count: 0
    .symbol:         _Z6gemm_gILi64ELi64ELi32ELi32ELi0ELi4ELi64ELi3EEv5GemmP.kd
    .uniform_work_group_size: 1
    .uses_dynamic_stack: false
    .vgpr_count:     52
    .vgpr_spill_count: 0
    .wavefront_size: 64
  - .agpr_count:     8
    .args:
      - .offset:         0
        .size:           112
        .value_kind:     by_value
    .group_segment_fixed_size: 73728
    .kernarg_segment_align: 8
    .kernarg_segment_size: 112
    .language:       OpenCL C
    .language_version:
      - 2
      - 0
    .max_flat_workgroup_size: 256
    .name:           _Z6gemm_gILi32ELi64ELi16ELi32ELi1ELi1ELi128ELi3EEv5GemmP
    .private_segment_fixed_size: 0
    .sgpr_count:     38
    .sgpr_spill_count: 0
    .symbol:         _Z6gemm_gILi32ELi64ELi16ELi32ELi1ELi1ELi128ELi3EEv5GemmP.kd
    .uniform_work_group_size: 1
    .uses_dynamic_stack: false
    .vgpr_count:     48
    .vgpr_spill_count: 0
    .wavefront_size: 64
  - .agpr_count:     0
    .args:
      - .offset:         0
        .size:           112
        .value_kind:     by_value
    .group_segment_fixed_size: 98304
    .kernarg_segment_align: 8
    .kernarg_segment_size: 112
    .language:       OpenCL C
    .language_version:
      - 2
      - 0
    .max_flat_workgroup_size: 256
    .name:           _Z6gemm_gILi32ELi64ELi16ELi32ELi1ELi1ELi64ELi4EEv5GemmP
    .private_segment_fixed_size: 0
    .sgpr_count:     36
    .sgpr_spill_count: 0
    .symbol:         _Z6gemm_gILi32ELi64ELi16ELi32ELi1ELi1ELi64ELi4EEv5GemmP.kd
    .uniform_work_group_size: 1
    .uses_dynamic_stack: false
    .vgpr_count:     148
    .vgpr_spill_count: 0
    .wavefront_size: 64
